# speedup vs baseline: 1.0108x; 1.0074x over previous
_Z7k1_projPKfPKDv8_DF16_S0_S0_S0_PS1_S4_S4_:
	s_load_dwordx8 s[12:19], s[0:1], 0x0
	s_load_dwordx8 s[4:11], s[0:1], 0x20
	v_mov_b32_e32 v182, v0
	v_and_b32_e32 v181, 63, v0
	v_lshrrev_b32_e32 v183, 6, v0
	v_lshlrev_b32_e32 v180, 4, v181
	s_lshr_b32 s20, s2, 6
	s_and_b32 s21, s2, 63
	v_readfirstlane_b32 s22, v183
	s_nop 3
	s_waitcnt lgkmcnt(0)
	s_cmp_lt_u32 s22, 4
	s_cbranch_scc0 .Lk1_loader
	s_lshl_b32 s23, s22, 15
	s_add_u32 s24, s14, s23
	s_addc_u32 s25, s15, 0
	s_add_u32 s26, s24, 0x20000
	s_addc_u32 s27, s25, 0
	s_add_u32 s28, s24, 0x40000
	s_addc_u32 s29, s25, 0
	s_cmp_lt_u32 s22, 2
	s_cselect_b32 s30, s16, s18
	s_cselect_b32 s31, s17, s19
	s_and_b32 s23, s22, 1
	s_lshl_b32 s23, s23, 7
	s_add_u32 s30, s30, s23
	s_addc_u32 s31, s31, 0
	v_lshrrev_b32_e32 v184, 5, v181
	v_lshlrev_b32_e32 v184, 4, v184
	global_load_dwordx4 v[0:3], v184, s[30:31] offset:0
	global_load_dwordx4 v[4:7], v184, s[30:31] offset:32
	global_load_dwordx4 v[8:11], v184, s[30:31] offset:64
	global_load_dwordx4 v[12:15], v184, s[30:31] offset:96
	v_and_b32_e32 v185, 31, v181
	v_lshlrev_b32_e32 v185, 2, v185
	s_lshl_b32 s23, s22, 7
	s_add_u32 s32, s4, s23
	s_addc_u32 s33, s5, 0
	global_load_dword v32, v185, s[32:33]
	global_load_dword v64, v185, s[32:33] offset:512
	global_load_dwordx4 v[96:99], v180, s[24:25] offset:0
	global_load_dwordx4 v[100:103], v180, s[26:27] offset:0
	global_load_dwordx4 v[104:107], v180, s[28:29] offset:0
	global_load_dwordx4 v[108:111], v180, s[24:25] offset:1024
	global_load_dwordx4 v[112:115], v180, s[26:27] offset:1024
	global_load_dwordx4 v[116:119], v180, s[28:29] offset:1024
	global_load_dwordx4 v[120:123], v180, s[24:25] offset:2048
	global_load_dwordx4 v[124:127], v180, s[26:27] offset:2048
	global_load_dwordx4 v[128:131], v180, s[28:29] offset:2048
	global_load_dwordx4 v[132:135], v180, s[24:25] offset:3072
	global_load_dwordx4 v[136:139], v180, s[26:27] offset:3072
	global_load_dwordx4 v[140:143], v180, s[28:29] offset:3072
	s_add_u32 s24, s24, 0x1000
	s_addc_u32 s25, s25, 0
	s_add_u32 s26, s26, 0x1000
	s_addc_u32 s27, s27, 0
	s_add_u32 s28, s28, 0x1000
	s_addc_u32 s29, s29, 0
	s_waitcnt vmcnt(12)
	v_mov_b32_e32 v16, v0
	v_mov_b32_e32 v17, v1
	v_mov_b32_e32 v18, v2
	v_mov_b32_e32 v19, v3
	v_mov_b32_e32 v20, v4
	v_mov_b32_e32 v21, v5
	v_mov_b32_e32 v22, v6
	v_mov_b32_e32 v23, v7
	v_mov_b32_e32 v24, v8
	v_mov_b32_e32 v25, v9
	v_mov_b32_e32 v26, v10
	v_mov_b32_e32 v27, v11
	v_mov_b32_e32 v28, v12
	v_mov_b32_e32 v29, v13
	v_mov_b32_e32 v30, v14
	v_mov_b32_e32 v31, v15
	v_mov_b32_e32 v33, v32
	v_mov_b32_e32 v34, v32
	v_mov_b32_e32 v35, v32
	v_mov_b32_e32 v36, v32
	v_mov_b32_e32 v37, v32
	v_mov_b32_e32 v38, v32
	v_mov_b32_e32 v39, v32
	v_mov_b32_e32 v40, v32
	v_mov_b32_e32 v41, v32
	v_mov_b32_e32 v42, v32
	v_mov_b32_e32 v43, v32
	v_mov_b32_e32 v44, v32
	v_mov_b32_e32 v45, v32
	v_mov_b32_e32 v46, v32
	v_mov_b32_e32 v47, v32
	v_mov_b32_e32 v48, v32
	v_mov_b32_e32 v49, v32
	v_mov_b32_e32 v50, v32
	v_mov_b32_e32 v51, v32
	v_mov_b32_e32 v52, v32
	v_mov_b32_e32 v53, v32
	v_mov_b32_e32 v54, v32
	v_mov_b32_e32 v55, v32
	v_mov_b32_e32 v56, v32
	v_mov_b32_e32 v57, v32
	v_mov_b32_e32 v58, v32
	v_mov_b32_e32 v59, v32
	v_mov_b32_e32 v60, v32
	v_mov_b32_e32 v61, v32
	v_mov_b32_e32 v62, v32
	v_mov_b32_e32 v63, v32
	v_mov_b32_e32 v65, v64
	v_mov_b32_e32 v66, v64
	v_mov_b32_e32 v67, v64
	v_mov_b32_e32 v68, v64
	v_mov_b32_e32 v69, v64
	v_mov_b32_e32 v70, v64
	v_mov_b32_e32 v71, v64
	v_mov_b32_e32 v72, v64
	v_mov_b32_e32 v73, v64
	v_mov_b32_e32 v74, v64
	v_mov_b32_e32 v75, v64
	v_mov_b32_e32 v76, v64
	v_mov_b32_e32 v77, v64
	v_mov_b32_e32 v78, v64
	v_mov_b32_e32 v79, v64
	v_mov_b32_e32 v80, v64
	v_mov_b32_e32 v81, v64
	v_mov_b32_e32 v82, v64
	v_mov_b32_e32 v83, v64
	v_mov_b32_e32 v84, v64
	v_mov_b32_e32 v85, v64
	v_mov_b32_e32 v86, v64
	v_mov_b32_e32 v87, v64
	v_mov_b32_e32 v88, v64
	v_mov_b32_e32 v89, v64
	v_mov_b32_e32 v90, v64
	v_mov_b32_e32 v91, v64
	v_mov_b32_e32 v92, v64
	v_mov_b32_e32 v93, v64
	v_mov_b32_e32 v94, v64
	v_mov_b32_e32 v95, v64
	s_barrier
	ds_read_b128 v[156:159], v180 offset:0
	ds_read_b128 v[160:163], v180 offset:32768
	ds_read_b128 v[164:167], v180 offset:1024
	ds_read_b128 v[168:171], v180 offset:33792
	global_load_dwordx4 v[144:147], v180, s[24:25] offset:0
	global_load_dwordx4 v[148:151], v180, s[26:27] offset:0
	global_load_dwordx4 v[152:155], v180, s[28:29] offset:0
	ds_read_b128 v[172:175], v180 offset:2048
	ds_read_b128 v[176:179], v180 offset:34816
	s_waitcnt vmcnt(12)
	s_waitcnt lgkmcnt(4)
	v_mfma_f32_32x32x16_f16 v[0:15], v[96:99], v[156:159], v[0:15]
	v_mfma_f32_32x32x16_f16 v[32:47], v[156:159], v[100:103], v[32:47]
	v_mfma_f32_32x32x16_f16 v[64:79], v[156:159], v[104:107], v[64:79]
	v_mfma_f32_32x32x16_f16 v[16:31], v[96:99], v[160:163], v[16:31]
	v_mfma_f32_32x32x16_f16 v[48:63], v[160:163], v[100:103], v[48:63]
	v_mfma_f32_32x32x16_f16 v[80:95], v[160:163], v[104:107], v[80:95]
	global_load_dwordx4 v[96:99], v180, s[24:25] offset:1024
	global_load_dwordx4 v[100:103], v180, s[26:27] offset:1024
	global_load_dwordx4 v[104:107], v180, s[28:29] offset:1024
	ds_read_b128 v[156:159], v180 offset:3072
	ds_read_b128 v[160:163], v180 offset:35840
	s_waitcnt vmcnt(12)
	s_waitcnt lgkmcnt(4)
	v_mfma_f32_32x32x16_f16 v[0:15], v[108:111], v[164:167], v[0:15]
	v_mfma_f32_32x32x16_f16 v[32:47], v[164:167], v[112:115], v[32:47]
	v_mfma_f32_32x32x16_f16 v[64:79], v[164:167], v[116:119], v[64:79]
	v_mfma_f32_32x32x16_f16 v[16:31], v[108:111], v[168:171], v[16:31]
	v_mfma_f32_32x32x16_f16 v[48:63], v[168:171], v[112:115], v[48:63]
	v_mfma_f32_32x32x16_f16 v[80:95], v[168:171], v[116:119], v[80:95]
	global_load_dwordx4 v[108:111], v180, s[24:25] offset:2048
	global_load_dwordx4 v[112:115], v180, s[26:27] offset:2048
	global_load_dwordx4 v[116:119], v180, s[28:29] offset:2048
	ds_read_b128 v[164:167], v180 offset:4096
	ds_read_b128 v[168:171], v180 offset:36864
	s_waitcnt vmcnt(12)
	s_waitcnt lgkmcnt(4)
	v_mfma_f32_32x32x16_f16 v[0:15], v[120:123], v[172:175], v[0:15]
	v_mfma_f32_32x32x16_f16 v[32:47], v[172:175], v[124:127], v[32:47]
	v_mfma_f32_32x32x16_f16 v[64:79], v[172:175], v[128:131], v[64:79]
	v_mfma_f32_32x32x16_f16 v[16:31], v[120:123], v[176:179], v[16:31]
	v_mfma_f32_32x32x16_f16 v[48:63], v[176:179], v[124:127], v[48:63]
	v_mfma_f32_32x32x16_f16 v[80:95], v[176:179], v[128:131], v[80:95]
	global_load_dwordx4 v[120:123], v180, s[24:25] offset:3072
	global_load_dwordx4 v[124:127], v180, s[26:27] offset:3072
	global_load_dwordx4 v[128:131], v180, s[28:29] offset:3072
	s_add_u32 s24, s24, 0x1000
	s_addc_u32 s25, s25, 0
	s_add_u32 s26, s26, 0x1000
	s_addc_u32 s27, s27, 0
	s_add_u32 s28, s28, 0x1000
	s_addc_u32 s29, s29, 0
	ds_read_b128 v[172:175], v180 offset:5120
	ds_read_b128 v[176:179], v180 offset:37888
	s_waitcnt vmcnt(12)
	s_waitcnt lgkmcnt(4)
	v_mfma_f32_32x32x16_f16 v[0:15], v[132:135], v[156:159], v[0:15]
	v_mfma_f32_32x32x16_f16 v[32:47], v[156:159], v[136:139], v[32:47]
	v_mfma_f32_32x32x16_f16 v[64:79], v[156:159], v[140:143], v[64:79]
	v_mfma_f32_32x32x16_f16 v[16:31], v[132:135], v[160:163], v[16:31]
	v_mfma_f32_32x32x16_f16 v[48:63], v[160:163], v[136:139], v[48:63]
	v_mfma_f32_32x32x16_f16 v[80:95], v[160:163], v[140:143], v[80:95]
	global_load_dwordx4 v[132:135], v180, s[24:25] offset:0
	global_load_dwordx4 v[136:139], v180, s[26:27] offset:0
	global_load_dwordx4 v[140:143], v180, s[28:29] offset:0
	ds_read_b128 v[156:159], v180 offset:6144
	ds_read_b128 v[160:163], v180 offset:38912
	s_waitcnt vmcnt(12)
	s_waitcnt lgkmcnt(4)
	v_mfma_f32_32x32x16_f16 v[0:15], v[144:147], v[164:167], v[0:15]
	v_mfma_f32_32x32x16_f16 v[32:47], v[164:167], v[148:151], v[32:47]
	v_mfma_f32_32x32x16_f16 v[64:79], v[164:167], v[152:155], v[64:79]
	v_mfma_f32_32x32x16_f16 v[16:31], v[144:147], v[168:171], v[16:31]
	v_mfma_f32_32x32x16_f16 v[48:63], v[168:171], v[148:151], v[48:63]
	v_mfma_f32_32x32x16_f16 v[80:95], v[168:171], v[152:155], v[80:95]
	global_load_dwordx4 v[144:147], v180, s[24:25] offset:1024
	global_load_dwordx4 v[148:151], v180, s[26:27] offset:1024
	global_load_dwordx4 v[152:155], v180, s[28:29] offset:1024
	ds_read_b128 v[164:167], v180 offset:7168
	ds_read_b128 v[168:171], v180 offset:39936
	s_waitcnt vmcnt(12)
	s_waitcnt lgkmcnt(4)
	v_mfma_f32_32x32x16_f16 v[0:15], v[96:99], v[172:175], v[0:15]
	v_mfma_f32_32x32x16_f16 v[32:47], v[172:175], v[100:103], v[32:47]
	v_mfma_f32_32x32x16_f16 v[64:79], v[172:175], v[104:107], v[64:79]
	v_mfma_f32_32x32x16_f16 v[16:31], v[96:99], v[176:179], v[16:31]
	v_mfma_f32_32x32x16_f16 v[48:63], v[176:179], v[100:103], v[48:63]
	v_mfma_f32_32x32x16_f16 v[80:95], v[176:179], v[104:107], v[80:95]
	global_load_dwordx4 v[96:99], v180, s[24:25] offset:2048
	global_load_dwordx4 v[100:103], v180, s[26:27] offset:2048
	global_load_dwordx4 v[104:107], v180, s[28:29] offset:2048
	s_waitcnt vmcnt(12)
	s_waitcnt lgkmcnt(2)
	v_mfma_f32_32x32x16_f16 v[0:15], v[108:111], v[156:159], v[0:15]
	v_mfma_f32_32x32x16_f16 v[32:47], v[156:159], v[112:115], v[32:47]
	v_mfma_f32_32x32x16_f16 v[64:79], v[156:159], v[116:119], v[64:79]
	v_mfma_f32_32x32x16_f16 v[16:31], v[108:111], v[160:163], v[16:31]
	v_mfma_f32_32x32x16_f16 v[48:63], v[160:163], v[112:115], v[48:63]
	v_mfma_f32_32x32x16_f16 v[80:95], v[160:163], v[116:119], v[80:95]
	global_load_dwordx4 v[108:111], v180, s[24:25] offset:3072
	global_load_dwordx4 v[112:115], v180, s[26:27] offset:3072
	global_load_dwordx4 v[116:119], v180, s[28:29] offset:3072
	s_add_u32 s24, s24, 0x1000
	s_addc_u32 s25, s25, 0
	s_add_u32 s26, s26, 0x1000
	s_addc_u32 s27, s27, 0
	s_add_u32 s28, s28, 0x1000
	s_addc_u32 s29, s29, 0
	s_waitcnt vmcnt(12)
	s_waitcnt lgkmcnt(0)
	v_mfma_f32_32x32x16_f16 v[0:15], v[120:123], v[164:167], v[0:15]
	v_mfma_f32_32x32x16_f16 v[32:47], v[164:167], v[124:127], v[32:47]
	v_mfma_f32_32x32x16_f16 v[64:79], v[164:167], v[128:131], v[64:79]
	v_mfma_f32_32x32x16_f16 v[16:31], v[120:123], v[168:171], v[16:31]
	v_mfma_f32_32x32x16_f16 v[48:63], v[168:171], v[124:127], v[48:63]
	v_mfma_f32_32x32x16_f16 v[80:95], v[168:171], v[128:131], v[80:95]
	s_barrier
	ds_read_b128 v[172:175], v180 offset:8192
	ds_read_b128 v[176:179], v180 offset:40960
	ds_read_b128 v[156:159], v180 offset:9216
	ds_read_b128 v[160:163], v180 offset:41984
	global_load_dwordx4 v[120:123], v180, s[24:25] offset:0
	global_load_dwordx4 v[124:127], v180, s[26:27] offset:0
	global_load_dwordx4 v[128:131], v180, s[28:29] offset:0
	ds_read_b128 v[164:167], v180 offset:10240
	ds_read_b128 v[168:171], v180 offset:43008
	s_waitcnt vmcnt(12)
	s_waitcnt lgkmcnt(4)
	v_mfma_f32_32x32x16_f16 v[0:15], v[132:135], v[172:175], v[0:15]
	v_mfma_f32_32x32x16_f16 v[32:47], v[172:175], v[136:139], v[32:47]
	v_mfma_f32_32x32x16_f16 v[64:79], v[172:175], v[140:143], v[64:79]
	v_mfma_f32_32x32x16_f16 v[16:31], v[132:135], v[176:179], v[16:31]
	v_mfma_f32_32x32x16_f16 v[48:63], v[176:179], v[136:139], v[48:63]
	v_mfma_f32_32x32x16_f16 v[80:95], v[176:179], v[140:143], v[80:95]
	global_load_dwordx4 v[132:135], v180, s[24:25] offset:1024
	global_load_dwordx4 v[136:139], v180, s[26:27] offset:1024
	global_load_dwordx4 v[140:143], v180, s[28:29] offset:1024
	ds_read_b128 v[172:175], v180 offset:11264
	ds_read_b128 v[176:179], v180 offset:44032
	s_waitcnt vmcnt(12)
	s_waitcnt lgkmcnt(4)
	v_mfma_f32_32x32x16_f16 v[0:15], v[144:147], v[156:159], v[0:15]
	v_mfma_f32_32x32x16_f16 v[32:47], v[156:159], v[148:151], v[32:47]
	v_mfma_f32_32x32x16_f16 v[64:79], v[156:159], v[152:155], v[64:79]
	v_mfma_f32_32x32x16_f16 v[16:31], v[144:147], v[160:163], v[16:31]
	v_mfma_f32_32x32x16_f16 v[48:63], v[160:163], v[148:151], v[48:63]
	v_mfma_f32_32x32x16_f16 v[80:95], v[160:163], v[152:155], v[80:95]
	global_load_dwordx4 v[144:147], v180, s[24:25] offset:2048
	global_load_dwordx4 v[148:151], v180, s[26:27] offset:2048
	global_load_dwordx4 v[152:155], v180, s[28:29] offset:2048
	ds_read_b128 v[156:159], v180 offset:12288
	ds_read_b128 v[160:163], v180 offset:45056
	s_waitcnt vmcnt(12)
	s_waitcnt lgkmcnt(4)
	v_mfma_f32_32x32x16_f16 v[0:15], v[96:99], v[164:167], v[0:15]
	v_mfma_f32_32x32x16_f16 v[32:47], v[164:167], v[100:103], v[32:47]
	v_mfma_f32_32x32x16_f16 v[64:79], v[164:167], v[104:107], v[64:79]
	v_mfma_f32_32x32x16_f16 v[16:31], v[96:99], v[168:171], v[16:31]
	v_mfma_f32_32x32x16_f16 v[48:63], v[168:171], v[100:103], v[48:63]
	v_mfma_f32_32x32x16_f16 v[80:95], v[168:171], v[104:107], v[80:95]
	global_load_dwordx4 v[96:99], v180, s[24:25] offset:3072
	global_load_dwordx4 v[100:103], v180, s[26:27] offset:3072
	global_load_dwordx4 v[104:107], v180, s[28:29] offset:3072
	s_add_u32 s24, s24, 0x1000
	s_addc_u32 s25, s25, 0
	s_add_u32 s26, s26, 0x1000
	s_addc_u32 s27, s27, 0
	s_add_u32 s28, s28, 0x1000
	s_addc_u32 s29, s29, 0
	ds_read_b128 v[164:167], v180 offset:13312
	ds_read_b128 v[168:171], v180 offset:46080
	s_waitcnt vmcnt(12)
	s_waitcnt lgkmcnt(4)
	v_mfma_f32_32x32x16_f16 v[0:15], v[108:111], v[172:175], v[0:15]
	v_mfma_f32_32x32x16_f16 v[32:47], v[172:175], v[112:115], v[32:47]
	v_mfma_f32_32x32x16_f16 v[64:79], v[172:175], v[116:119], v[64:79]
	v_mfma_f32_32x32x16_f16 v[16:31], v[108:111], v[176:179], v[16:31]
	v_mfma_f32_32x32x16_f16 v[48:63], v[176:179], v[112:115], v[48:63]
	v_mfma_f32_32x32x16_f16 v[80:95], v[176:179], v[116:119], v[80:95]
	global_load_dwordx4 v[108:111], v180, s[24:25] offset:0
	global_load_dwordx4 v[112:115], v180, s[26:27] offset:0
	global_load_dwordx4 v[116:119], v180, s[28:29] offset:0
	ds_read_b128 v[172:175], v180 offset:14336
	ds_read_b128 v[176:179], v180 offset:47104
	s_waitcnt vmcnt(12)
	s_waitcnt lgkmcnt(4)
	v_mfma_f32_32x32x16_f16 v[0:15], v[120:123], v[156:159], v[0:15]
	v_mfma_f32_32x32x16_f16 v[32:47], v[156:159], v[124:127], v[32:47]
	v_mfma_f32_32x32x16_f16 v[64:79], v[156:159], v[128:131], v[64:79]
	v_mfma_f32_32x32x16_f16 v[16:31], v[120:123], v[160:163], v[16:31]
	v_mfma_f32_32x32x16_f16 v[48:63], v[160:163], v[124:127], v[48:63]
	v_mfma_f32_32x32x16_f16 v[80:95], v[160:163], v[128:131], v[80:95]
	global_load_dwordx4 v[120:123], v180, s[24:25] offset:1024
	global_load_dwordx4 v[124:127], v180, s[26:27] offset:1024
	global_load_dwordx4 v[128:131], v180, s[28:29] offset:1024
	ds_read_b128 v[156:159], v180 offset:15360
	ds_read_b128 v[160:163], v180 offset:48128
	s_waitcnt vmcnt(12)
	s_waitcnt lgkmcnt(4)
	v_mfma_f32_32x32x16_f16 v[0:15], v[132:135], v[164:167], v[0:15]
	v_mfma_f32_32x32x16_f16 v[32:47], v[164:167], v[136:139], v[32:47]
	v_mfma_f32_32x32x16_f16 v[64:79], v[164:167], v[140:143], v[64:79]
	v_mfma_f32_32x32x16_f16 v[16:31], v[132:135], v[168:171], v[16:31]
	v_mfma_f32_32x32x16_f16 v[48:63], v[168:171], v[136:139], v[48:63]
	v_mfma_f32_32x32x16_f16 v[80:95], v[168:171], v[140:143], v[80:95]
	global_load_dwordx4 v[132:135], v180, s[24:25] offset:2048
	global_load_dwordx4 v[136:139], v180, s[26:27] offset:2048
	global_load_dwordx4 v[140:143], v180, s[28:29] offset:2048
	s_waitcnt vmcnt(12)
	s_waitcnt lgkmcnt(2)
	v_mfma_f32_32x32x16_f16 v[0:15], v[144:147], v[172:175], v[0:15]
	v_mfma_f32_32x32x16_f16 v[32:47], v[172:175], v[148:151], v[32:47]
	v_mfma_f32_32x32x16_f16 v[64:79], v[172:175], v[152:155], v[64:79]
	v_mfma_f32_32x32x16_f16 v[16:31], v[144:147], v[176:179], v[16:31]
	v_mfma_f32_32x32x16_f16 v[48:63], v[176:179], v[148:151], v[48:63]
	v_mfma_f32_32x32x16_f16 v[80:95], v[176:179], v[152:155], v[80:95]
	global_load_dwordx4 v[144:147], v180, s[24:25] offset:3072
	global_load_dwordx4 v[148:151], v180, s[26:27] offset:3072
	global_load_dwordx4 v[152:155], v180, s[28:29] offset:3072
	s_add_u32 s24, s24, 0x1000
	s_addc_u32 s25, s25, 0
	s_add_u32 s26, s26, 0x1000
	s_addc_u32 s27, s27, 0
	s_add_u32 s28, s28, 0x1000
	s_addc_u32 s29, s29, 0
	s_waitcnt vmcnt(12)
	s_waitcnt lgkmcnt(0)
	v_mfma_f32_32x32x16_f16 v[0:15], v[96:99], v[156:159], v[0:15]
	v_mfma_f32_32x32x16_f16 v[32:47], v[156:159], v[100:103], v[32:47]
	v_mfma_f32_32x32x16_f16 v[64:79], v[156:159], v[104:107], v[64:79]
	v_mfma_f32_32x32x16_f16 v[16:31], v[96:99], v[160:163], v[16:31]
	v_mfma_f32_32x32x16_f16 v[48:63], v[160:163], v[100:103], v[48:63]
	v_mfma_f32_32x32x16_f16 v[80:95], v[160:163], v[104:107], v[80:95]
	s_barrier
	ds_read_b128 v[164:167], v180 offset:16384
	ds_read_b128 v[168:171], v180 offset:49152
	ds_read_b128 v[172:175], v180 offset:17408
	ds_read_b128 v[176:179], v180 offset:50176
	global_load_dwordx4 v[96:99], v180, s[24:25] offset:0
	global_load_dwordx4 v[100:103], v180, s[26:27] offset:0
	global_load_dwordx4 v[104:107], v180, s[28:29] offset:0
	ds_read_b128 v[156:159], v180 offset:18432
	ds_read_b128 v[160:163], v180 offset:51200
	s_waitcnt vmcnt(12)
	s_waitcnt lgkmcnt(4)
	v_mfma_f32_32x32x16_f16 v[0:15], v[108:111], v[164:167], v[0:15]
	v_mfma_f32_32x32x16_f16 v[32:47], v[164:167], v[112:115], v[32:47]
	v_mfma_f32_32x32x16_f16 v[64:79], v[164:167], v[116:119], v[64:79]
	v_mfma_f32_32x32x16_f16 v[16:31], v[108:111], v[168:171], v[16:31]
	v_mfma_f32_32x32x16_f16 v[48:63], v[168:171], v[112:115], v[48:63]
	v_mfma_f32_32x32x16_f16 v[80:95], v[168:171], v[116:119], v[80:95]
	global_load_dwordx4 v[108:111], v180, s[24:25] offset:1024
	global_load_dwordx4 v[112:115], v180, s[26:27] offset:1024
	global_load_dwordx4 v[116:119], v180, s[28:29] offset:1024
	ds_read_b128 v[164:167], v180 offset:19456
	ds_read_b128 v[168:171], v180 offset:52224
	s_waitcnt vmcnt(12)
	s_waitcnt lgkmcnt(4)
	v_mfma_f32_32x32x16_f16 v[0:15], v[120:123], v[172:175], v[0:15]
	v_mfma_f32_32x32x16_f16 v[32:47], v[172:175], v[124:127], v[32:47]
	v_mfma_f32_32x32x16_f16 v[64:79], v[172:175], v[128:131], v[64:79]
	v_mfma_f32_32x32x16_f16 v[16:31], v[120:123], v[176:179], v[16:31]
	v_mfma_f32_32x32x16_f16 v[48:63], v[176:179], v[124:127], v[48:63]
	v_mfma_f32_32x32x16_f16 v[80:95], v[176:179], v[128:131], v[80:95]
	global_load_dwordx4 v[120:123], v180, s[24:25] offset:2048
	global_load_dwordx4 v[124:127], v180, s[26:27] offset:2048
	global_load_dwordx4 v[128:131], v180, s[28:29] offset:2048
	ds_read_b128 v[172:175], v180 offset:20480
	ds_read_b128 v[176:179], v180 offset:53248
	s_waitcnt vmcnt(12)
	s_waitcnt lgkmcnt(4)
	v_mfma_f32_32x32x16_f16 v[0:15], v[132:135], v[156:159], v[0:15]
	v_mfma_f32_32x32x16_f16 v[32:47], v[156:159], v[136:139], v[32:47]
	v_mfma_f32_32x32x16_f16 v[64:79], v[156:159], v[140:143], v[64:79]
	v_mfma_f32_32x32x16_f16 v[16:31], v[132:135], v[160:163], v[16:31]
	v_mfma_f32_32x32x16_f16 v[48:63], v[160:163], v[136:139], v[48:63]
	v_mfma_f32_32x32x16_f16 v[80:95], v[160:163], v[140:143], v[80:95]
	global_load_dwordx4 v[132:135], v180, s[24:25] offset:3072
	global_load_dwordx4 v[136:139], v180, s[26:27] offset:3072
	global_load_dwordx4 v[140:143], v180, s[28:29] offset:3072
	s_add_u32 s24, s24, 0x1000
	s_addc_u32 s25, s25, 0
	s_add_u32 s26, s26, 0x1000
	s_addc_u32 s27, s27, 0
	s_add_u32 s28, s28, 0x1000
	s_addc_u32 s29, s29, 0
	ds_read_b128 v[156:159], v180 offset:21504
	ds_read_b128 v[160:163], v180 offset:54272
	s_waitcnt vmcnt(12)
	s_waitcnt lgkmcnt(4)
	v_mfma_f32_32x32x16_f16 v[0:15], v[144:147], v[164:167], v[0:15]
	v_mfma_f32_32x32x16_f16 v[32:47], v[164:167], v[148:151], v[32:47]
	v_mfma_f32_32x32x16_f16 v[64:79], v[164:167], v[152:155], v[64:79]
	v_mfma_f32_32x32x16_f16 v[16:31], v[144:147], v[168:171], v[16:31]
	v_mfma_f32_32x32x16_f16 v[48:63], v[168:171], v[148:151], v[48:63]
	v_mfma_f32_32x32x16_f16 v[80:95], v[168:171], v[152:155], v[80:95]
	global_load_dwordx4 v[144:147], v180, s[24:25] offset:0
	global_load_dwordx4 v[148:151], v180, s[26:27] offset:0
	global_load_dwordx4 v[152:155], v180, s[28:29] offset:0
	ds_read_b128 v[164:167], v180 offset:22528
	ds_read_b128 v[168:171], v180 offset:55296
	s_waitcnt vmcnt(12)
	s_waitcnt lgkmcnt(4)
	v_mfma_f32_32x32x16_f16 v[0:15], v[96:99], v[172:175], v[0:15]
	v_mfma_f32_32x32x16_f16 v[32:47], v[172:175], v[100:103], v[32:47]
	v_mfma_f32_32x32x16_f16 v[64:79], v[172:175], v[104:107], v[64:79]
	v_mfma_f32_32x32x16_f16 v[16:31], v[96:99], v[176:179], v[16:31]
	v_mfma_f32_32x32x16_f16 v[48:63], v[176:179], v[100:103], v[48:63]
	v_mfma_f32_32x32x16_f16 v[80:95], v[176:179], v[104:107], v[80:95]
	global_load_dwordx4 v[96:99], v180, s[24:25] offset:1024
	global_load_dwordx4 v[100:103], v180, s[26:27] offset:1024
	global_load_dwordx4 v[104:107], v180, s[28:29] offset:1024
	ds_read_b128 v[172:175], v180 offset:23552
	ds_read_b128 v[176:179], v180 offset:56320
	s_waitcnt vmcnt(12)
	s_waitcnt lgkmcnt(4)
	v_mfma_f32_32x32x16_f16 v[0:15], v[108:111], v[156:159], v[0:15]
	v_mfma_f32_32x32x16_f16 v[32:47], v[156:159], v[112:115], v[32:47]
	v_mfma_f32_32x32x16_f16 v[64:79], v[156:159], v[116:119], v[64:79]
	v_mfma_f32_32x32x16_f16 v[16:31], v[108:111], v[160:163], v[16:31]
	v_mfma_f32_32x32x16_f16 v[48:63], v[160:163], v[112:115], v[48:63]
	v_mfma_f32_32x32x16_f16 v[80:95], v[160:163], v[116:119], v[80:95]
	global_load_dwordx4 v[108:111], v180, s[24:25] offset:2048
	global_load_dwordx4 v[112:115], v180, s[26:27] offset:2048
	global_load_dwordx4 v[116:119], v180, s[28:29] offset:2048
	s_waitcnt vmcnt(12)
	s_waitcnt lgkmcnt(2)
	v_mfma_f32_32x32x16_f16 v[0:15], v[120:123], v[164:167], v[0:15]
	v_mfma_f32_32x32x16_f16 v[32:47], v[164:167], v[124:127], v[32:47]
	v_mfma_f32_32x32x16_f16 v[64:79], v[164:167], v[128:131], v[64:79]
	v_mfma_f32_32x32x16_f16 v[16:31], v[120:123], v[168:171], v[16:31]
	v_mfma_f32_32x32x16_f16 v[48:63], v[168:171], v[124:127], v[48:63]
	v_mfma_f32_32x32x16_f16 v[80:95], v[168:171], v[128:131], v[80:95]
	global_load_dwordx4 v[120:123], v180, s[24:25] offset:3072
	global_load_dwordx4 v[124:127], v180, s[26:27] offset:3072
	global_load_dwordx4 v[128:131], v180, s[28:29] offset:3072
	s_add_u32 s24, s24, 0x1000
	s_addc_u32 s25, s25, 0
	s_add_u32 s26, s26, 0x1000
	s_addc_u32 s27, s27, 0
	s_add_u32 s28, s28, 0x1000
	s_addc_u32 s29, s29, 0
	s_waitcnt vmcnt(12)
	s_waitcnt lgkmcnt(0)
	v_mfma_f32_32x32x16_f16 v[0:15], v[132:135], v[172:175], v[0:15]
	v_mfma_f32_32x32x16_f16 v[32:47], v[172:175], v[136:139], v[32:47]
	v_mfma_f32_32x32x16_f16 v[64:79], v[172:175], v[140:143], v[64:79]
	v_mfma_f32_32x32x16_f16 v[16:31], v[132:135], v[176:179], v[16:31]
	v_mfma_f32_32x32x16_f16 v[48:63], v[176:179], v[136:139], v[48:63]
	v_mfma_f32_32x32x16_f16 v[80:95], v[176:179], v[140:143], v[80:95]
	s_barrier
	ds_read_b128 v[156:159], v180 offset:24576
	ds_read_b128 v[160:163], v180 offset:57344
	ds_read_b128 v[164:167], v180 offset:25600
	ds_read_b128 v[168:171], v180 offset:58368
	global_load_dwordx4 v[132:135], v180, s[24:25] offset:0
	global_load_dwordx4 v[136:139], v180, s[26:27] offset:0
	global_load_dwordx4 v[140:143], v180, s[28:29] offset:0
	ds_read_b128 v[172:175], v180 offset:26624
	ds_read_b128 v[176:179], v180 offset:59392
	s_waitcnt vmcnt(12)
	s_waitcnt lgkmcnt(4)
	v_mfma_f32_32x32x16_f16 v[0:15], v[144:147], v[156:159], v[0:15]
	v_mfma_f32_32x32x16_f16 v[32:47], v[156:159], v[148:151], v[32:47]
	v_mfma_f32_32x32x16_f16 v[64:79], v[156:159], v[152:155], v[64:79]
	v_mfma_f32_32x32x16_f16 v[16:31], v[144:147], v[160:163], v[16:31]
	v_mfma_f32_32x32x16_f16 v[48:63], v[160:163], v[148:151], v[48:63]
	v_mfma_f32_32x32x16_f16 v[80:95], v[160:163], v[152:155], v[80:95]
	global_load_dwordx4 v[144:147], v180, s[24:25] offset:1024
	global_load_dwordx4 v[148:151], v180, s[26:27] offset:1024
	global_load_dwordx4 v[152:155], v180, s[28:29] offset:1024
	ds_read_b128 v[156:159], v180 offset:27648
	ds_read_b128 v[160:163], v180 offset:60416
	s_waitcnt vmcnt(12)
	s_waitcnt lgkmcnt(4)
	v_mfma_f32_32x32x16_f16 v[0:15], v[96:99], v[164:167], v[0:15]
	v_mfma_f32_32x32x16_f16 v[32:47], v[164:167], v[100:103], v[32:47]
	v_mfma_f32_32x32x16_f16 v[64:79], v[164:167], v[104:107], v[64:79]
	v_mfma_f32_32x32x16_f16 v[16:31], v[96:99], v[168:171], v[16:31]
	v_mfma_f32_32x32x16_f16 v[48:63], v[168:171], v[100:103], v[48:63]
	v_mfma_f32_32x32x16_f16 v[80:95], v[168:171], v[104:107], v[80:95]
	global_load_dwordx4 v[96:99], v180, s[24:25] offset:2048
	global_load_dwordx4 v[100:103], v180, s[26:27] offset:2048
	global_load_dwordx4 v[104:107], v180, s[28:29] offset:2048
	ds_read_b128 v[164:167], v180 offset:28672
	ds_read_b128 v[168:171], v180 offset:61440
	s_waitcnt vmcnt(12)
	s_waitcnt lgkmcnt(4)
	v_mfma_f32_32x32x16_f16 v[0:15], v[108:111], v[172:175], v[0:15]
	v_mfma_f32_32x32x16_f16 v[32:47], v[172:175], v[112:115], v[32:47]
	v_mfma_f32_32x32x16_f16 v[64:79], v[172:175], v[116:119], v[64:79]
	v_mfma_f32_32x32x16_f16 v[16:31], v[108:111], v[176:179], v[16:31]
	v_mfma_f32_32x32x16_f16 v[48:63], v[176:179], v[112:115], v[48:63]
	v_mfma_f32_32x32x16_f16 v[80:95], v[176:179], v[116:119], v[80:95]
	global_load_dwordx4 v[108:111], v180, s[24:25] offset:3072
	global_load_dwordx4 v[112:115], v180, s[26:27] offset:3072
	global_load_dwordx4 v[116:119], v180, s[28:29] offset:3072
	s_add_u32 s24, s24, 0x1000
	s_addc_u32 s25, s25, 0
	s_add_u32 s26, s26, 0x1000
	s_addc_u32 s27, s27, 0
	s_add_u32 s28, s28, 0x1000
	s_addc_u32 s29, s29, 0
	ds_read_b128 v[172:175], v180 offset:29696
	ds_read_b128 v[176:179], v180 offset:62464
	s_waitcnt vmcnt(12)
	s_waitcnt lgkmcnt(4)
	v_mfma_f32_32x32x16_f16 v[0:15], v[120:123], v[156:159], v[0:15]
	v_mfma_f32_32x32x16_f16 v[32:47], v[156:159], v[124:127], v[32:47]
	v_mfma_f32_32x32x16_f16 v[64:79], v[156:159], v[128:131], v[64:79]
	v_mfma_f32_32x32x16_f16 v[16:31], v[120:123], v[160:163], v[16:31]
	v_mfma_f32_32x32x16_f16 v[48:63], v[160:163], v[124:127], v[48:63]
	v_mfma_f32_32x32x16_f16 v[80:95], v[160:163], v[128:131], v[80:95]
	ds_read_b128 v[156:159], v180 offset:30720
	ds_read_b128 v[160:163], v180 offset:63488
	s_waitcnt vmcnt(9)
	s_waitcnt lgkmcnt(4)
	v_mfma_f32_32x32x16_f16 v[0:15], v[132:135], v[164:167], v[0:15]
	v_mfma_f32_32x32x16_f16 v[32:47], v[164:167], v[136:139], v[32:47]
	v_mfma_f32_32x32x16_f16 v[64:79], v[164:167], v[140:143], v[64:79]
	v_mfma_f32_32x32x16_f16 v[16:31], v[132:135], v[168:171], v[16:31]
	v_mfma_f32_32x32x16_f16 v[48:63], v[168:171], v[136:139], v[48:63]
	v_mfma_f32_32x32x16_f16 v[80:95], v[168:171], v[140:143], v[80:95]
	ds_read_b128 v[164:167], v180 offset:31744
	ds_read_b128 v[168:171], v180 offset:64512
	s_waitcnt vmcnt(6)
	s_waitcnt lgkmcnt(4)
	v_mfma_f32_32x32x16_f16 v[0:15], v[144:147], v[172:175], v[0:15]
	v_mfma_f32_32x32x16_f16 v[32:47], v[172:175], v[148:151], v[32:47]
	v_mfma_f32_32x32x16_f16 v[64:79], v[172:175], v[152:155], v[64:79]
	v_mfma_f32_32x32x16_f16 v[16:31], v[144:147], v[176:179], v[16:31]
	v_mfma_f32_32x32x16_f16 v[48:63], v[176:179], v[148:151], v[48:63]
	v_mfma_f32_32x32x16_f16 v[80:95], v[176:179], v[152:155], v[80:95]
	s_waitcnt vmcnt(3)
	s_waitcnt lgkmcnt(2)
	v_mfma_f32_32x32x16_f16 v[0:15], v[96:99], v[156:159], v[0:15]
	v_mfma_f32_32x32x16_f16 v[32:47], v[156:159], v[100:103], v[32:47]
	v_mfma_f32_32x32x16_f16 v[64:79], v[156:159], v[104:107], v[64:79]
	v_mfma_f32_32x32x16_f16 v[16:31], v[96:99], v[160:163], v[16:31]
	v_mfma_f32_32x32x16_f16 v[48:63], v[160:163], v[100:103], v[48:63]
	v_mfma_f32_32x32x16_f16 v[80:95], v[160:163], v[104:107], v[80:95]
	s_waitcnt vmcnt(0)
	s_waitcnt lgkmcnt(0)
	v_mfma_f32_32x32x16_f16 v[0:15], v[108:111], v[164:167], v[0:15]
	v_mfma_f32_32x32x16_f16 v[32:47], v[164:167], v[112:115], v[32:47]
	v_mfma_f32_32x32x16_f16 v[64:79], v[164:167], v[116:119], v[64:79]
	v_mfma_f32_32x32x16_f16 v[16:31], v[108:111], v[168:171], v[16:31]
	v_mfma_f32_32x32x16_f16 v[48:63], v[168:171], v[112:115], v[48:63]
	v_mfma_f32_32x32x16_f16 v[80:95], v[168:171], v[116:119], v[80:95]
	s_lshl_b32 s34, s20, 7
	s_lshl_b32 s35, s21, 1
	s_add_u32 s34, s34, s35
	s_cmp_lt_u32 s22, 2
	s_cselect_b32 s36, s6, s8
	s_cselect_b32 s37, s7, s9
	s_cselect_b32 s38, 0x3fb8aa3b, 1.0
	s_lshl_b32 s39, s34, 12
	s_and_b32 s23, s22, 1
	s_lshl_b32 s23, s23, 11
	s_add_u32 s39, s39, s23
	v_add_u32_e32 v186, s39, v180
	s_lshl_b32 s40, s34, 14
	s_lshl_b32 s23, s22, 11
	s_add_u32 s40, s40, s23
	v_add_u32_e32 v187, s40, v180
	s_nop 7
	s_nop 7
	v_mul_f32_e32 v0, 0x4038aa3b, v0
	v_mul_f32_e32 v1, 0x4038aa3b, v1
	v_mul_f32_e32 v2, 0x4038aa3b, v2
	v_mul_f32_e32 v3, 0x4038aa3b, v3
	v_mul_f32_e32 v4, 0x4038aa3b, v4
	v_mul_f32_e32 v5, 0x4038aa3b, v5
	v_mul_f32_e32 v6, 0x4038aa3b, v6
	v_mul_f32_e32 v7, 0x4038aa3b, v7
	v_mul_f32_e32 v8, 0x4038aa3b, v8
	v_mul_f32_e32 v9, 0x4038aa3b, v9
	v_mul_f32_e32 v10, 0x4038aa3b, v10
	v_mul_f32_e32 v11, 0x4038aa3b, v11
	v_mul_f32_e32 v12, 0x4038aa3b, v12
	v_mul_f32_e32 v13, 0x4038aa3b, v13
	v_mul_f32_e32 v14, 0x4038aa3b, v14
	v_mul_f32_e32 v15, 0x4038aa3b, v15
	v_exp_f32_e32 v0, v0
	v_exp_f32_e32 v1, v1
	v_exp_f32_e32 v2, v2
	v_exp_f32_e32 v3, v3
	v_exp_f32_e32 v4, v4
	v_exp_f32_e32 v5, v5
	v_exp_f32_e32 v6, v6
	v_exp_f32_e32 v7, v7
	v_exp_f32_e32 v8, v8
	v_exp_f32_e32 v9, v9
	v_exp_f32_e32 v10, v10
	v_exp_f32_e32 v11, v11
	v_exp_f32_e32 v12, v12
	v_exp_f32_e32 v13, v13
	v_exp_f32_e32 v14, v14
	v_exp_f32_e32 v15, v15
	s_nop 0
	v_add_f32_e32 v0, 1.0, v0
	v_add_f32_e32 v1, 1.0, v1
	v_add_f32_e32 v2, 1.0, v2
	v_add_f32_e32 v3, 1.0, v3
	v_add_f32_e32 v4, 1.0, v4
	v_add_f32_e32 v5, 1.0, v5
	v_add_f32_e32 v6, 1.0, v6
	v_add_f32_e32 v7, 1.0, v7
	v_add_f32_e32 v8, 1.0, v8
	v_add_f32_e32 v9, 1.0, v9
	v_add_f32_e32 v10, 1.0, v10
	v_add_f32_e32 v11, 1.0, v11
	v_add_f32_e32 v12, 1.0, v12
	v_add_f32_e32 v13, 1.0, v13
	v_add_f32_e32 v14, 1.0, v14
	v_add_f32_e32 v15, 1.0, v15
	v_rcp_f32_e32 v0, v0
	v_rcp_f32_e32 v1, v1
	v_rcp_f32_e32 v2, v2
	v_rcp_f32_e32 v3, v3
	v_rcp_f32_e32 v4, v4
	v_rcp_f32_e32 v5, v5
	v_rcp_f32_e32 v6, v6
	v_rcp_f32_e32 v7, v7
	v_rcp_f32_e32 v8, v8
	v_rcp_f32_e32 v9, v9
	v_rcp_f32_e32 v10, v10
	v_rcp_f32_e32 v11, v11
	v_rcp_f32_e32 v12, v12
	v_rcp_f32_e32 v13, v13
	v_rcp_f32_e32 v14, v14
	v_rcp_f32_e32 v15, v15
	s_nop 0
	v_fma_f32 v0, -v0, 2.0, 1.0
	v_fma_f32 v1, -v1, 2.0, 1.0
	v_fma_f32 v2, -v2, 2.0, 1.0
	v_fma_f32 v3, -v3, 2.0, 1.0
	v_fma_f32 v4, -v4, 2.0, 1.0
	v_fma_f32 v5, -v5, 2.0, 1.0
	v_fma_f32 v6, -v6, 2.0, 1.0
	v_fma_f32 v7, -v7, 2.0, 1.0
	v_fma_f32 v8, -v8, 2.0, 1.0
	v_fma_f32 v9, -v9, 2.0, 1.0
	v_fma_f32 v10, -v10, 2.0, 1.0
	v_fma_f32 v11, -v11, 2.0, 1.0
	v_fma_f32 v12, -v12, 2.0, 1.0
	v_fma_f32 v13, -v13, 2.0, 1.0
	v_fma_f32 v14, -v14, 2.0, 1.0
	v_fma_f32 v15, -v15, 2.0, 1.0
	v_mul_f32_e32 v0, s38, v0
	v_mul_f32_e32 v1, s38, v1
	v_mul_f32_e32 v2, s38, v2
	v_mul_f32_e32 v3, s38, v3
	v_mul_f32_e32 v4, s38, v4
	v_mul_f32_e32 v5, s38, v5
	v_mul_f32_e32 v6, s38, v6
	v_mul_f32_e32 v7, s38, v7
	v_mul_f32_e32 v8, s38, v8
	v_mul_f32_e32 v9, s38, v9
	v_mul_f32_e32 v10, s38, v10
	v_mul_f32_e32 v11, s38, v11
	v_mul_f32_e32 v12, s38, v12
	v_mul_f32_e32 v13, s38, v13
	v_mul_f32_e32 v14, s38, v14
	v_mul_f32_e32 v15, s38, v15
	v_cvt_pk_f16_f32 v96, v0, v1
	v_cvt_pk_f16_f32 v97, v2, v3
	v_cvt_pk_f16_f32 v98, v4, v5
	v_cvt_pk_f16_f32 v99, v6, v7
	v_cvt_pk_f16_f32 v100, v8, v9
	v_cvt_pk_f16_f32 v101, v10, v11
	v_cvt_pk_f16_f32 v102, v12, v13
	v_cvt_pk_f16_f32 v103, v14, v15
	global_store_dwordx4 v186, v[96:99], s[36:37] sc1
	global_store_dwordx4 v186, v[100:103], s[36:37] offset:1024 sc1
	v_mul_f32_e32 v16, 0x4038aa3b, v16
	v_mul_f32_e32 v17, 0x4038aa3b, v17
	v_mul_f32_e32 v18, 0x4038aa3b, v18
	v_mul_f32_e32 v19, 0x4038aa3b, v19
	v_mul_f32_e32 v20, 0x4038aa3b, v20
	v_mul_f32_e32 v21, 0x4038aa3b, v21
	v_mul_f32_e32 v22, 0x4038aa3b, v22
	v_mul_f32_e32 v23, 0x4038aa3b, v23
	v_mul_f32_e32 v24, 0x4038aa3b, v24
	v_mul_f32_e32 v25, 0x4038aa3b, v25
	v_mul_f32_e32 v26, 0x4038aa3b, v26
	v_mul_f32_e32 v27, 0x4038aa3b, v27
	v_mul_f32_e32 v28, 0x4038aa3b, v28
	v_mul_f32_e32 v29, 0x4038aa3b, v29
	v_mul_f32_e32 v30, 0x4038aa3b, v30
	v_mul_f32_e32 v31, 0x4038aa3b, v31
	v_exp_f32_e32 v16, v16
	v_exp_f32_e32 v17, v17
	v_exp_f32_e32 v18, v18
	v_exp_f32_e32 v19, v19
	v_exp_f32_e32 v20, v20
	v_exp_f32_e32 v21, v21
	v_exp_f32_e32 v22, v22
	v_exp_f32_e32 v23, v23
	v_exp_f32_e32 v24, v24
	v_exp_f32_e32 v25, v25
	v_exp_f32_e32 v26, v26
	v_exp_f32_e32 v27, v27
	v_exp_f32_e32 v28, v28
	v_exp_f32_e32 v29, v29
	v_exp_f32_e32 v30, v30
	v_exp_f32_e32 v31, v31
	s_nop 0
	v_add_f32_e32 v16, 1.0, v16
	v_add_f32_e32 v17, 1.0, v17
	v_add_f32_e32 v18, 1.0, v18
	v_add_f32_e32 v19, 1.0, v19
	v_add_f32_e32 v20, 1.0, v20
	v_add_f32_e32 v21, 1.0, v21
	v_add_f32_e32 v22, 1.0, v22
	v_add_f32_e32 v23, 1.0, v23
	v_add_f32_e32 v24, 1.0, v24
	v_add_f32_e32 v25, 1.0, v25
	v_add_f32_e32 v26, 1.0, v26
	v_add_f32_e32 v27, 1.0, v27
	v_add_f32_e32 v28, 1.0, v28
	v_add_f32_e32 v29, 1.0, v29
	v_add_f32_e32 v30, 1.0, v30
	v_add_f32_e32 v31, 1.0, v31
	v_rcp_f32_e32 v16, v16
	v_rcp_f32_e32 v17, v17
	v_rcp_f32_e32 v18, v18
	v_rcp_f32_e32 v19, v19
	v_rcp_f32_e32 v20, v20
	v_rcp_f32_e32 v21, v21
	v_rcp_f32_e32 v22, v22
	v_rcp_f32_e32 v23, v23
	v_rcp_f32_e32 v24, v24
	v_rcp_f32_e32 v25, v25
	v_rcp_f32_e32 v26, v26
	v_rcp_f32_e32 v27, v27
	v_rcp_f32_e32 v28, v28
	v_rcp_f32_e32 v29, v29
	v_rcp_f32_e32 v30, v30
	v_rcp_f32_e32 v31, v31
	s_nop 0
	v_fma_f32 v16, -v16, 2.0, 1.0
	v_fma_f32 v17, -v17, 2.0, 1.0
	v_fma_f32 v18, -v18, 2.0, 1.0
	v_fma_f32 v19, -v19, 2.0, 1.0
	v_fma_f32 v20, -v20, 2.0, 1.0
	v_fma_f32 v21, -v21, 2.0, 1.0
	v_fma_f32 v22, -v22, 2.0, 1.0
	v_fma_f32 v23, -v23, 2.0, 1.0
	v_fma_f32 v24, -v24, 2.0, 1.0
	v_fma_f32 v25, -v25, 2.0, 1.0
	v_fma_f32 v26, -v26, 2.0, 1.0
	v_fma_f32 v27, -v27, 2.0, 1.0
	v_fma_f32 v28, -v28, 2.0, 1.0
	v_fma_f32 v29, -v29, 2.0, 1.0
	v_fma_f32 v30, -v30, 2.0, 1.0
	v_fma_f32 v31, -v31, 2.0, 1.0
	v_mul_f32_e32 v16, s38, v16
	v_mul_f32_e32 v17, s38, v17
	v_mul_f32_e32 v18, s38, v18
	v_mul_f32_e32 v19, s38, v19
	v_mul_f32_e32 v20, s38, v20
	v_mul_f32_e32 v21, s38, v21
	v_mul_f32_e32 v22, s38, v22
	v_mul_f32_e32 v23, s38, v23
	v_mul_f32_e32 v24, s38, v24
	v_mul_f32_e32 v25, s38, v25
	v_mul_f32_e32 v26, s38, v26
	v_mul_f32_e32 v27, s38, v27
	v_mul_f32_e32 v28, s38, v28
	v_mul_f32_e32 v29, s38, v29
	v_mul_f32_e32 v30, s38, v30
	v_mul_f32_e32 v31, s38, v31
	v_cvt_pk_f16_f32 v104, v16, v17
	v_cvt_pk_f16_f32 v105, v18, v19
	v_cvt_pk_f16_f32 v106, v20, v21
	v_cvt_pk_f16_f32 v107, v22, v23
	v_cvt_pk_f16_f32 v108, v24, v25
	v_cvt_pk_f16_f32 v109, v26, v27
	v_cvt_pk_f16_f32 v110, v28, v29
	v_cvt_pk_f16_f32 v111, v30, v31
	v_add_u32_e32 v186, 0x1000, v186
	global_store_dwordx4 v186, v[104:107], s[36:37] sc1
	global_store_dwordx4 v186, v[108:111], s[36:37] offset:1024 sc1
	v_add_u32_e32 v188, 0x2000, v187
	v_add_u32_e32 v189, 0x4000, v187
	v_add_u32_e32 v190, 0x4000, v188
	v_cvt_pk_f16_f32 v112, v32, v33
	v_cvt_pk_f16_f32 v113, v34, v35
	v_cvt_pk_f16_f32 v114, v36, v37
	v_cvt_pk_f16_f32 v115, v38, v39
	global_store_dwordx4 v187, v[112:115], s[10:11] offset:0 sc1
	v_cvt_pk_f16_f32 v116, v40, v41
	v_cvt_pk_f16_f32 v117, v42, v43
	v_cvt_pk_f16_f32 v118, v44, v45
	v_cvt_pk_f16_f32 v119, v46, v47
	global_store_dwordx4 v187, v[116:119], s[10:11] offset:1024 sc1
	v_cvt_pk_f16_f32 v120, v48, v49
	v_cvt_pk_f16_f32 v121, v50, v51
	v_cvt_pk_f16_f32 v122, v52, v53
	v_cvt_pk_f16_f32 v123, v54, v55
	global_store_dwordx4 v189, v[120:123], s[10:11] offset:0 sc1
	v_cvt_pk_f16_f32 v124, v56, v57
	v_cvt_pk_f16_f32 v125, v58, v59
	v_cvt_pk_f16_f32 v126, v60, v61
	v_cvt_pk_f16_f32 v127, v62, v63
	global_store_dwordx4 v189, v[124:127], s[10:11] offset:1024 sc1
	v_cvt_pk_f16_f32 v128, v64, v65
	v_cvt_pk_f16_f32 v129, v66, v67
	v_cvt_pk_f16_f32 v130, v68, v69
	v_cvt_pk_f16_f32 v131, v70, v71
	global_store_dwordx4 v188, v[128:131], s[10:11] offset:0 sc1
	v_cvt_pk_f16_f32 v132, v72, v73
	v_cvt_pk_f16_f32 v133, v74, v75
	v_cvt_pk_f16_f32 v134, v76, v77
	v_cvt_pk_f16_f32 v135, v78, v79
	global_store_dwordx4 v188, v[132:135], s[10:11] offset:1024 sc1
	v_cvt_pk_f16_f32 v136, v80, v81
	v_cvt_pk_f16_f32 v137, v82, v83
	v_cvt_pk_f16_f32 v138, v84, v85
	v_cvt_pk_f16_f32 v139, v86, v87
	global_store_dwordx4 v190, v[136:139], s[10:11] offset:0 sc1
	v_cvt_pk_f16_f32 v140, v88, v89
	v_cvt_pk_f16_f32 v141, v90, v91
	v_cvt_pk_f16_f32 v142, v92, v93
	v_cvt_pk_f16_f32 v143, v94, v95
	global_store_dwordx4 v190, v[140:143], s[10:11] offset:1024 sc1
	s_endpgm
